# layer0 gather: 3 rotating edge slots in flight per 16-lane group (was 2), fits in 64 VGPRs
# speedup vs baseline: 1.0065x; 1.0065x over previous
.LBB4_45:
	v_mov_b32_e32 v17, v30
	v_or_b32_e32 v14, 1, v31
	v_add_u32_e32 v14, s30, v14
	v_min_i32_e32 v14, 0x1869f, v14
	v_lshl_add_u32 v14, v14, 8, v26
	global_load_dwordx4 v[10:13], v14, s[24:25]
	s_mov_b64 s[28:29], exec
	s_movk_i32 s0, 0x4400
	v_subrev_u32_e32 v1, s20, v32
	v_lshl_add_u32 v1, v1, 2, s0
	v_lshl_add_u32 v16, v32, 8, v26
	v_cmp_lt_i32_e64 s[2:3], v32, v33
	v_add_u32_e32 v14, 1, v32
	v_cmp_lt_i32_e64 s[8:9], v14, v33
	v_add_u32_e32 v14, 2, v32
	v_cmp_lt_i32_e64 s[10:11], v14, v33
	s_mov_b64 exec, s[2:3]
	ds_read_b32 v18, v1 offset:0
	ds_read_b32 v19, v1 offset:4096
	s_waitcnt lgkmcnt(0)
	v_lshl_add_u32 v18, v18, 9, v26
	v_lshl_add_u32 v19, v19, 8, v26
	global_load_dwordx4 v[34:37], v18, s[4:5] offset:256 nt
	global_load_dwordx4 v[20:23], v18, s[4:5] nt
	global_load_dwordx4 v[38:41], v19, s[24:25]
	ds_read_b32 v18, v1 offset:12
	ds_read_b32 v19, v1 offset:4108
	s_mov_b64 exec, s[28:29]
	global_load_dword v27, v26, s[24:25]
	s_mov_b64 exec, s[8:9]
	ds_read_b32 v24, v1 offset:4
	ds_read_b32 v25, v1 offset:4100
	s_waitcnt lgkmcnt(0)
	v_lshl_add_u32 v24, v24, 9, v26
	v_lshl_add_u32 v25, v25, 8, v26
	global_load_dwordx4 v[50:53], v24, s[4:5] offset:256 nt
	global_load_dwordx4 v[46:49], v24, s[4:5] nt
	global_load_dwordx4 v[54:57], v25, s[24:25]
	ds_read_b32 v24, v1 offset:16
	ds_read_b32 v25, v1 offset:4112
	s_mov_b64 exec, s[28:29]
	global_load_dword v27, v26, s[24:25]
	s_mov_b64 exec, s[10:11]
	ds_read_b32 v62, v1 offset:8
	ds_read_b32 v63, v1 offset:4104
	s_waitcnt lgkmcnt(0)
	v_lshl_add_u32 v62, v62, 9, v26
	v_lshl_add_u32 v63, v63, 8, v26
	global_load_dwordx4 v[42:45], v62, s[4:5] offset:256 nt
	global_load_dwordx4 v[58:61], v62, s[4:5] nt
	global_load_dwordx4 v[28:31], v63, s[24:25]
	ds_read_b32 v62, v1 offset:20
	ds_read_b32 v63, v1 offset:4116
	s_mov_b64 exec, s[28:29]
	s_cmp_eq_u64 s[2:3], 0
	s_cbranch_scc1 .Ll0_p1_empty
.Ll0_p1_loop:
	s_mov_b64 exec, s[2:3]
	s_waitcnt vmcnt(8)
	v_cvt_pk_f16_f32 v20, v20, v21
	v_cvt_pk_f16_f32 v21, v22, v23
	v_cvt_pk_f16_f32 v22, v34, v35
	v_cvt_pk_f16_f32 v23, v36, v37
	global_store_dwordx4 v16, v[20:23], s[6:7] offset:0 sc1
	v_fma_mix_f32 v14, v38, 1.0, v20 op_sel_hi:[1,0,1]
	v_fma_mix_f32 v15, v38, 1.0, v20 op_sel:[1,0,1] op_sel_hi:[1,0,1]
	v_max_f32_e32 v14, 0, v14
	v_max_f32_e32 v15, 0, v15
	v_pk_add_f32 v[2:3], v[2:3], v[14:15]
	v_fma_mix_f32 v14, v39, 1.0, v21 op_sel_hi:[1,0,1]
	v_fma_mix_f32 v15, v39, 1.0, v21 op_sel:[1,0,1] op_sel_hi:[1,0,1]
	v_max_f32_e32 v14, 0, v14
	v_max_f32_e32 v15, 0, v15
	v_pk_add_f32 v[4:5], v[4:5], v[14:15]
	v_fma_mix_f32 v14, v40, 1.0, v22 op_sel_hi:[1,0,1]
	v_fma_mix_f32 v15, v40, 1.0, v22 op_sel:[1,0,1] op_sel_hi:[1,0,1]
	v_max_f32_e32 v14, 0, v14
	v_max_f32_e32 v15, 0, v15
	v_pk_add_f32 v[6:7], v[6:7], v[14:15]
	v_fma_mix_f32 v14, v41, 1.0, v23 op_sel_hi:[1,0,1]
	v_fma_mix_f32 v15, v41, 1.0, v23 op_sel:[1,0,1] op_sel_hi:[1,0,1]
	v_max_f32_e32 v14, 0, v14
	v_max_f32_e32 v15, 0, v15
	v_pk_add_f32 v[8:9], v[8:9], v[14:15]
	v_add_u32_e32 v14, 3, v32
	v_cmp_lt_i32_e64 s[2:3], v14, v33
	s_mov_b64 exec, s[2:3]
	s_waitcnt lgkmcnt(0)
	v_lshl_add_u32 v18, v18, 9, v26
	v_lshl_add_u32 v19, v19, 8, v26
	global_load_dwordx4 v[34:37], v18, s[4:5] offset:256 nt
	global_load_dwordx4 v[20:23], v18, s[4:5] nt
	global_load_dwordx4 v[38:41], v19, s[24:25]
	ds_read_b32 v18, v1 offset:24
	ds_read_b32 v19, v1 offset:4120
	s_mov_b64 exec, s[8:9]
	s_waitcnt vmcnt(8)
	v_cvt_pk_f16_f32 v46, v46, v47
	v_cvt_pk_f16_f32 v47, v48, v49
	v_cvt_pk_f16_f32 v48, v50, v51
	v_cvt_pk_f16_f32 v49, v52, v53
	global_store_dwordx4 v16, v[46:49], s[6:7] offset:256 sc1
	v_fma_mix_f32 v14, v54, 1.0, v46 op_sel_hi:[1,0,1]
	v_fma_mix_f32 v15, v54, 1.0, v46 op_sel:[1,0,1] op_sel_hi:[1,0,1]
	v_max_f32_e32 v14, 0, v14
	v_max_f32_e32 v15, 0, v15
	v_pk_add_f32 v[2:3], v[2:3], v[14:15]
	v_fma_mix_f32 v14, v55, 1.0, v47 op_sel_hi:[1,0,1]
	v_fma_mix_f32 v15, v55, 1.0, v47 op_sel:[1,0,1] op_sel_hi:[1,0,1]
	v_max_f32_e32 v14, 0, v14
	v_max_f32_e32 v15, 0, v15
	v_pk_add_f32 v[4:5], v[4:5], v[14:15]
	v_fma_mix_f32 v14, v56, 1.0, v48 op_sel_hi:[1,0,1]
	v_fma_mix_f32 v15, v56, 1.0, v48 op_sel:[1,0,1] op_sel_hi:[1,0,1]
	v_max_f32_e32 v14, 0, v14
	v_max_f32_e32 v15, 0, v15
	v_pk_add_f32 v[6:7], v[6:7], v[14:15]
	v_fma_mix_f32 v14, v57, 1.0, v49 op_sel_hi:[1,0,1]
	v_fma_mix_f32 v15, v57, 1.0, v49 op_sel:[1,0,1] op_sel_hi:[1,0,1]
	v_max_f32_e32 v14, 0, v14
	v_max_f32_e32 v15, 0, v15
	v_pk_add_f32 v[8:9], v[8:9], v[14:15]
	v_add_u32_e32 v14, 4, v32
	v_cmp_lt_i32_e64 s[8:9], v14, v33
	s_mov_b64 exec, s[8:9]
	s_waitcnt lgkmcnt(0)
	v_lshl_add_u32 v24, v24, 9, v26
	v_lshl_add_u32 v25, v25, 8, v26
	global_load_dwordx4 v[50:53], v24, s[4:5] offset:256 nt
	global_load_dwordx4 v[46:49], v24, s[4:5] nt
	global_load_dwordx4 v[54:57], v25, s[24:25]
	ds_read_b32 v24, v1 offset:28
	ds_read_b32 v25, v1 offset:4124
	s_mov_b64 exec, s[10:11]
	s_waitcnt vmcnt(8)
	v_cvt_pk_f16_f32 v58, v58, v59
	v_cvt_pk_f16_f32 v59, v60, v61
	v_cvt_pk_f16_f32 v60, v42, v43
	v_cvt_pk_f16_f32 v61, v44, v45
	global_store_dwordx4 v16, v[58:61], s[6:7] offset:512 sc1
	v_fma_mix_f32 v14, v28, 1.0, v58 op_sel_hi:[1,0,1]
	v_fma_mix_f32 v15, v28, 1.0, v58 op_sel:[1,0,1] op_sel_hi:[1,0,1]
	v_max_f32_e32 v14, 0, v14
	v_max_f32_e32 v15, 0, v15
	v_pk_add_f32 v[2:3], v[2:3], v[14:15]
	v_fma_mix_f32 v14, v29, 1.0, v59 op_sel_hi:[1,0,1]
	v_fma_mix_f32 v15, v29, 1.0, v59 op_sel:[1,0,1] op_sel_hi:[1,0,1]
	v_max_f32_e32 v14, 0, v14
	v_max_f32_e32 v15, 0, v15
	v_pk_add_f32 v[4:5], v[4:5], v[14:15]
	v_fma_mix_f32 v14, v30, 1.0, v60 op_sel_hi:[1,0,1]
	v_fma_mix_f32 v15, v30, 1.0, v60 op_sel:[1,0,1] op_sel_hi:[1,0,1]
	v_max_f32_e32 v14, 0, v14
	v_max_f32_e32 v15, 0, v15
	v_pk_add_f32 v[6:7], v[6:7], v[14:15]
	v_fma_mix_f32 v14, v31, 1.0, v61 op_sel_hi:[1,0,1]
	v_fma_mix_f32 v15, v31, 1.0, v61 op_sel:[1,0,1] op_sel_hi:[1,0,1]
	v_max_f32_e32 v14, 0, v14
	v_max_f32_e32 v15, 0, v15
	v_pk_add_f32 v[8:9], v[8:9], v[14:15]
	v_add_u32_e32 v14, 5, v32
	v_cmp_lt_i32_e64 s[10:11], v14, v33
	s_mov_b64 exec, s[10:11]
	s_waitcnt lgkmcnt(0)
	v_lshl_add_u32 v62, v62, 9, v26
	v_lshl_add_u32 v63, v63, 8, v26
	global_load_dwordx4 v[42:45], v62, s[4:5] offset:256 nt
	global_load_dwordx4 v[58:61], v62, s[4:5] nt
	global_load_dwordx4 v[28:31], v63, s[24:25]
	ds_read_b32 v62, v1 offset:32
	ds_read_b32 v63, v1 offset:4128
	s_mov_b64 exec, s[28:29]
	v_add_u32_e32 v32, 3, v32
	v_add_u32_e32 v1, 12, v1
	v_add_u32_e32 v16, 0x300, v16
	s_cmp_lg_u64 s[2:3], 0
	s_cbranch_scc1 .Ll0_p1_loop
	s_branch .Ll0_p1_done

.Ll0_p1_done:
	s_movk_i32 s2, 0x110
	v_cvt_pk_f16_f32 v21, v8, v9
	v_cvt_pk_f16_f32 v20, v6, v7
	v_cvt_pk_f16_f32 v19, v4, v5
	v_cvt_pk_f16_f32 v18, v2, v3
	v_lshrrev_b32_e32 v15, 3, v0
	v_and_b32_e32 v14, 62, v15
	v_mad_u32_u24 v14, v14, s2, v26
	ds_write_b128 v14, v[18:21]
	v_or_b32_e32 v15, 1, v15
	v_mov_b32_e32 v14, 0x6400
	v_lshl_or_b32 v14, v15, 2, v14
	ds_read2_b32 v[32:33], v14 offset1:1
	v_add_u32_e32 v14, s30, v15
	s_mov_b32 s2, 0x186a0
	v_cmp_gt_i32_e32 vcc, s2, v14
	v_cvt_f32_f16_e32 v2, v10
	v_cvt_f32_f16_sdwa v3, v10 dst_sel:DWORD dst_unused:UNUSED_PAD src0_sel:WORD_1
	v_cvt_f32_f16_e32 v4, v11
	v_cvt_f32_f16_sdwa v5, v11 dst_sel:DWORD dst_unused:UNUSED_PAD src0_sel:WORD_1
	v_cvt_f32_f16_e32 v6, v12
	v_cvt_f32_f16_sdwa v7, v12 dst_sel:DWORD dst_unused:UNUSED_PAD src0_sel:WORD_1
	v_cvt_f32_f16_e32 v8, v13
	v_cvt_f32_f16_sdwa v9, v13 dst_sel:DWORD dst_unused:UNUSED_PAD src0_sel:WORD_1
	v_mul_f32_e32 v2, v17, v2
	v_mul_f32_e32 v3, v17, v3
	v_mul_f32_e32 v4, v17, v4
	v_mul_f32_e32 v5, v17, v5
	v_mul_f32_e32 v6, v17, v6
	v_mul_f32_e32 v7, v17, v7
	v_mul_f32_e32 v8, v17, v8
	v_mul_f32_e32 v9, v17, v9
	v_cndmask_b32_e32 v2, 0, v2, vcc
	v_cndmask_b32_e32 v3, 0, v3, vcc
	v_cndmask_b32_e32 v4, 0, v4, vcc
	v_cndmask_b32_e32 v5, 0, v5, vcc
	v_cndmask_b32_e32 v6, 0, v6, vcc
	v_cndmask_b32_e32 v7, 0, v7, vcc
	v_cndmask_b32_e32 v8, 0, v8, vcc
	v_cndmask_b32_e32 v9, 0, v9, vcc
	s_waitcnt lgkmcnt(0)
	v_subrev_u32_e32 v1, s20, v32
	v_lshl_add_u32 v1, v1, 2, s0
	v_lshl_add_u32 v16, v32, 8, v26
	v_cmp_lt_i32_e64 s[2:3], v32, v33
	v_add_u32_e32 v14, 1, v32
	v_cmp_lt_i32_e64 s[8:9], v14, v33
	v_add_u32_e32 v14, 2, v32
	v_cmp_lt_i32_e64 s[10:11], v14, v33
	s_mov_b64 exec, s[2:3]
	ds_read_b32 v18, v1 offset:0
	ds_read_b32 v19, v1 offset:4096
	s_waitcnt lgkmcnt(0)
	v_lshl_add_u32 v18, v18, 9, v26
	v_lshl_add_u32 v19, v19, 8, v26
	global_load_dwordx4 v[34:37], v18, s[4:5] offset:256 nt
	global_load_dwordx4 v[20:23], v18, s[4:5] nt
	global_load_dwordx4 v[38:41], v19, s[24:25]
	ds_read_b32 v18, v1 offset:12
	ds_read_b32 v19, v1 offset:4108
	s_mov_b64 exec, s[28:29]
	global_load_dword v27, v26, s[24:25]
	s_mov_b64 exec, s[8:9]
	ds_read_b32 v24, v1 offset:4
	ds_read_b32 v25, v1 offset:4100
	s_waitcnt lgkmcnt(0)
	v_lshl_add_u32 v24, v24, 9, v26
	v_lshl_add_u32 v25, v25, 8, v26
	global_load_dwordx4 v[50:53], v24, s[4:5] offset:256 nt
	global_load_dwordx4 v[46:49], v24, s[4:5] nt
	global_load_dwordx4 v[54:57], v25, s[24:25]
	ds_read_b32 v24, v1 offset:16
	ds_read_b32 v25, v1 offset:4112
	s_mov_b64 exec, s[28:29]
	global_load_dword v27, v26, s[24:25]
	s_mov_b64 exec, s[10:11]
	ds_read_b32 v62, v1 offset:8
	ds_read_b32 v63, v1 offset:4104
	s_waitcnt lgkmcnt(0)
	v_lshl_add_u32 v62, v62, 9, v26
	v_lshl_add_u32 v63, v63, 8, v26
	global_load_dwordx4 v[42:45], v62, s[4:5] offset:256 nt
	global_load_dwordx4 v[58:61], v62, s[4:5] nt
	global_load_dwordx4 v[28:31], v63, s[24:25]
	ds_read_b32 v62, v1 offset:20
	ds_read_b32 v63, v1 offset:4116
	s_mov_b64 exec, s[28:29]
	s_cmp_eq_u64 s[2:3], 0
	s_cbranch_scc1 .Ll0_p2_empty

.Ll0_p2_done:
	v_mov_b64_e32 v[16:17], v[8:9]
	v_mov_b64_e32 v[14:15], v[6:7]
	v_mov_b64_e32 v[12:13], v[4:5]
	v_mov_b64_e32 v[10:11], v[2:3]
	v_lshrrev_b32_e32 v1, 3, v0
	v_or_b32_e32 v1, 1, v1
	v_and_b32_e32 v42, 15, v0
	v_mbcnt_lo_u32_b32 v43, -1, 0
	s_branch .LBB4_70

	.amdhsa_kernel _Z12layer_kernelILb1ELi512ELi64EEvPKDv8_DF16_PKfPS0_PiS6_S6_S2_S4_S5_PfPK15HIP_vector_typeIiLj2EEPKi
		.amdhsa_group_segment_fixed_size 26384
		.amdhsa_private_segment_fixed_size 0
		.amdhsa_kernarg_size 352
		.amdhsa_user_sgpr_count 2
		.amdhsa_user_sgpr_dispatch_ptr 0
		.amdhsa_user_sgpr_queue_ptr 0
		.amdhsa_user_sgpr_kernarg_segment_ptr 1
		.amdhsa_user_sgpr_dispatch_id 0
		.amdhsa_user_sgpr_kernarg_preload_length 0
		.amdhsa_user_sgpr_kernarg_preload_offset 0
		.amdhsa_user_sgpr_private_segment_size 0
		.amdhsa_uses_dynamic_stack 0
		.amdhsa_enable_private_segment 0
		.amdhsa_system_sgpr_workgroup_id_x 1
		.amdhsa_system_sgpr_workgroup_id_y 0
		.amdhsa_system_sgpr_workgroup_id_z 0
		.amdhsa_system_sgpr_workgroup_info 0
		.amdhsa_system_vgpr_workitem_id 0
		.amdhsa_next_free_vgpr 64
		.amdhsa_next_free_sgpr 46
		.amdhsa_accum_offset 64
		.amdhsa_reserve_vcc 1
		.amdhsa_float_round_mode_32 0
		.amdhsa_float_round_mode_16_64 0
		.amdhsa_float_denorm_mode_32 3
		.amdhsa_float_denorm_mode_16_64 3
		.amdhsa_dx10_clamp 1
		.amdhsa_ieee_mode 1
		.amdhsa_fp16_overflow 0
		.amdhsa_tg_split 0
		.amdhsa_exception_fp_ieee_invalid_op 0
		.amdhsa_exception_fp_denorm_src 0
		.amdhsa_exception_fp_ieee_div_zero 0
		.amdhsa_exception_fp_ieee_overflow 0
		.amdhsa_exception_fp_ieee_underflow 0
		.amdhsa_exception_fp_ieee_inexact 0
		.amdhsa_exception_int_div_zero 0
	.end_amdhsa_kernel

amdhsa.kernels:
  - .agpr_count:     0
    .args:
      - .actual_access:  read_only
        .address_space:  global
        .offset:         0
        .size:           8
        .value_kind:     global_buffer
      - .address_space:  global
        .offset:         8
        .size:           8
        .value_kind:     global_buffer
      - .actual_access:  read_only
        .address_space:  global
        .offset:         16
        .size:           8
        .value_kind:     global_buffer
      - .actual_access:  read_only
        .address_space:  global
        .offset:         24
        .size:           8
        .value_kind:     global_buffer
      - .actual_access:  write_only
        .address_space:  global
        .offset:         32
        .size:           8
        .value_kind:     global_buffer
      - .actual_access:  read_only
        .address_space:  global
        .offset:         40
        .size:           8
        .value_kind:     global_buffer
      - .actual_access:  write_only
        .address_space:  global
        .offset:         48
        .size:           8
        .value_kind:     global_buffer
      - .actual_access:  write_only
        .address_space:  global
        .offset:         56
        .size:           8
        .value_kind:     global_buffer
    .group_segment_fixed_size: 6400
    .kernarg_segment_align: 8
    .kernarg_segment_size: 64
    .language:       OpenCL C
    .language_version:
      - 2
      - 0
    .max_flat_workgroup_size: 1024
    .name:           _Z17prep_count_kernelPKfPDv8_DF16_S0_S0_S2_PKiPiP15HIP_vector_typeIfLj4EE
    .private_segment_fixed_size: 0
    .sgpr_count:     22
    .sgpr_spill_count: 0
    .symbol:         _Z17prep_count_kernelPKfPDv8_DF16_S0_S0_S2_PKiPiP15HIP_vector_typeIfLj4EE.kd
    .uniform_work_group_size: 1
    .uses_dynamic_stack: false
    .vgpr_count:     22
    .vgpr_spill_count: 0
    .wavefront_size: 64
  - .agpr_count:     0
    .args:
      - .actual_access:  read_only
        .address_space:  global
        .offset:         0
        .size:           8
        .value_kind:     global_buffer
      - .actual_access:  read_only
        .address_space:  global
        .offset:         8
        .size:           8
        .value_kind:     global_buffer
      - .actual_access:  read_only
        .address_space:  global
        .offset:         16
        .size:           8
        .value_kind:     global_buffer
      - .actual_access:  write_only
        .address_space:  global
        .offset:         24
        .size:           8
        .value_kind:     global_buffer
      - .actual_access:  write_only
        .address_space:  global
        .offset:         32
        .size:           8
        .value_kind:     global_buffer
    .group_segment_fixed_size: 124704
    .kernarg_segment_align: 8
    .kernarg_segment_size: 40
    .language:       OpenCL C
    .language_version:
      - 2
      - 0
    .max_flat_workgroup_size: 1024
    .name:           _Z14scatter_kernelPKiS0_S0_PiP15HIP_vector_typeIiLj2EE
    .private_segment_fixed_size: 0
    .sgpr_count:     55
    .sgpr_spill_count: 0
    .symbol:         _Z14scatter_kernelPKiS0_S0_PiP15HIP_vector_typeIiLj2EE.kd
    .uniform_work_group_size: 1
    .uses_dynamic_stack: false
    .vgpr_count:     128
    .vgpr_spill_count: 0
    .wavefront_size: 64
  - .agpr_count:     0
    .args:
      - .actual_access:  read_only
        .address_space:  global
        .offset:         0
        .size:           8
        .value_kind:     global_buffer
      - .address_space:  global
        .offset:         8
        .size:           8
        .value_kind:     global_buffer
      - .address_space:  global
        .offset:         16
        .size:           8
        .value_kind:     global_buffer
      - .actual_access:  read_only
        .address_space:  global
        .offset:         24
        .size:           8
        .value_kind:     global_buffer
      - .actual_access:  read_only
        .address_space:  global
        .offset:         32
        .size:           8
        .value_kind:     global_buffer
      - .actual_access:  read_only
        .address_space:  global
        .offset:         40
        .size:           8
        .value_kind:     global_buffer
      - .offset:         48
        .size:           4
        .value_kind:     hidden_block_count_x
      - .offset:         52
        .size:           4
        .value_kind:     hidden_block_count_y
      - .offset:         56
        .size:           4
        .value_kind:     hidden_block_count_z
      - .offset:         60
        .size:           2
        .value_kind:     hidden_group_size_x
      - .offset:         62
        .size:           2
        .value_kind:     hidden_group_size_y
      - .offset:         64
        .size:           2
        .value_kind:     hidden_group_size_z
      - .offset:         66
        .size:           2
        .value_kind:     hidden_remainder_x
      - .offset:         68
        .size:           2
        .value_kind:     hidden_remainder_y
      - .offset:         70
        .size:           2
        .value_kind:     hidden_remainder_z
      - .offset:         88
        .size:           8
        .value_kind:     hidden_global_offset_x
      - .offset:         96
        .size:           8
        .value_kind:     hidden_global_offset_y
      - .offset:         104
        .size:           8
        .value_kind:     hidden_global_offset_z
      - .offset:         112
        .size:           2
        .value_kind:     hidden_grid_dims
    .group_segment_fixed_size: 1024
    .kernarg_segment_align: 8
    .kernarg_segment_size: 304
    .language:       OpenCL C
    .language_version:
      - 2
      - 0
    .max_flat_workgroup_size: 256
    .name:           _Z9bn_kernelPKDv8_DF16_S1_PS_PKfS4_S4_
    .private_segment_fixed_size: 0
    .sgpr_count:     20
    .sgpr_spill_count: 0
    .symbol:         _Z9bn_kernelPKDv8_DF16_S1_PS_PKfS4_S4_.kd
    .uniform_work_group_size: 1
    .uses_dynamic_stack: false
    .vgpr_count:     64
    .vgpr_spill_count: 0
    .wavefront_size: 64
  - .agpr_count:     0
    .args:
      - .actual_access:  read_only
        .address_space:  global
        .offset:         0
        .size:           8
        .value_kind:     global_buffer
      - .actual_access:  read_only
        .address_space:  global
        .offset:         8
        .size:           8
        .value_kind:     global_buffer
      - .actual_access:  read_only
        .address_space:  global
        .offset:         16
        .size:           8
        .value_kind:     global_buffer
      - .actual_access:  read_only
        .address_space:  global
        .offset:         24
        .size:           8
        .value_kind:     global_buffer
      - .actual_access:  read_only
        .address_space:  global
        .offset:         32
        .size:           8
        .value_kind:     global_buffer
      - .actual_access:  read_only
        .address_space:  global
        .offset:         40
        .size:           8
        .value_kind:     global_buffer
      - .actual_access:  read_only
        .address_space:  global
        .offset:         48
        .size:           8
        .value_kind:     global_buffer
      - .actual_access:  write_only
        .address_space:  global
        .offset:         56
        .size:           8
        .value_kind:     global_buffer
      - .offset:         64
        .size:           4
        .value_kind:     hidden_block_count_x
      - .offset:         68
        .size:           4
        .value_kind:     hidden_block_count_y
      - .offset:         72
        .size:           4
        .value_kind:     hidden_block_count_z
      - .offset:         76
        .size:           2
        .value_kind:     hidden_group_size_x
      - .offset:         78
        .size:           2
        .value_kind:     hidden_group_size_y
      - .offset:         80
        .size:           2
        .value_kind:     hidden_group_size_z
      - .offset:         82
        .size:           2
        .value_kind:     hidden_remainder_x
      - .offset:         84
        .size:           2
        .value_kind:     hidden_remainder_y
      - .offset:         86
        .size:           2
        .value_kind:     hidden_remainder_z
      - .offset:         104
        .size:           8
        .value_kind:     hidden_global_offset_x
      - .offset:         112
        .size:           8
        .value_kind:     hidden_global_offset_y
      - .offset:         120
        .size:           8
        .value_kind:     hidden_global_offset_z
      - .offset:         128
        .size:           2
        .value_kind:     hidden_grid_dims
    .group_segment_fixed_size: 34816
    .kernarg_segment_align: 8
    .kernarg_segment_size: 320
    .language:       OpenCL C
    .language_version:
      - 2
      - 0
    .max_flat_workgroup_size: 512
    .name:           _Z12final_kernelPKDv8_DF16_S1_PKfS3_S3_S1_S3_Pf
    .private_segment_fixed_size: 0
    .sgpr_count:     34
    .sgpr_spill_count: 0
    .symbol:         _Z12final_kernelPKDv8_DF16_S1_PKfS3_S3_S1_S3_Pf.kd
    .uniform_work_group_size: 1
    .uses_dynamic_stack: false
    .vgpr_count:     60
    .vgpr_spill_count: 0
    .wavefront_size: 64
  - .agpr_count:     0
    .args:
      - .actual_access:  read_only
        .address_space:  global
        .offset:         0
        .size:           8
        .value_kind:     global_buffer
      - .actual_access:  read_only
        .address_space:  global
        .offset:         8
        .size:           8
        .value_kind:     global_buffer
      - .address_space:  global
        .offset:         16
        .size:           8
        .value_kind:     global_buffer
      - .actual_access:  write_only
        .address_space:  global
        .offset:         24
        .size:           8
        .value_kind:     global_buffer
      - .address_space:  global
        .offset:         32
        .size:           8
        .value_kind:     global_buffer
      - .address_space:  global
        .offset:         40
        .size:           8
        .value_kind:     global_buffer
      - .actual_access:  read_only
        .address_space:  global
        .offset:         48
        .size:           8
        .value_kind:     global_buffer
      - .actual_access:  read_only
        .address_space:  global
        .offset:         56
        .size:           8
        .value_kind:     global_buffer
      - .address_space:  global
        .offset:         64
        .size:           8
        .value_kind:     global_buffer
      - .address_space:  global
        .offset:         72
        .size:           8
        .value_kind:     global_buffer
      - .actual_access:  read_only
        .address_space:  global
        .offset:         80
        .size:           8
        .value_kind:     global_buffer
      - .actual_access:  read_only
        .address_space:  global
        .offset:         88
        .size:           8
        .value_kind:     global_buffer
      - .offset:         96
        .size:           4
        .value_kind:     hidden_block_count_x
      - .offset:         100
        .size:           4
        .value_kind:     hidden_block_count_y
      - .offset:         104
        .size:           4
        .value_kind:     hidden_block_count_z
      - .offset:         108
        .size:           2
        .value_kind:     hidden_group_size_x
      - .offset:         110
        .size:           2
        .value_kind:     hidden_group_size_y
      - .offset:         112
        .size:           2
        .value_kind:     hidden_group_size_z
      - .offset:         114
        .size:           2
        .value_kind:     hidden_remainder_x
      - .offset:         116
        .size:           2
        .value_kind:     hidden_remainder_y
      - .offset:         118
        .size:           2
        .value_kind:     hidden_remainder_z
      - .offset:         136
        .size:           8
        .value_kind:     hidden_global_offset_x
      - .offset:         144
        .size:           8
        .value_kind:     hidden_global_offset_y
      - .offset:         152
        .size:           8
        .value_kind:     hidden_global_offset_z
      - .offset:         160
        .size:           2
        .value_kind:     hidden_grid_dims
    .group_segment_fixed_size: 26384
    .kernarg_segment_align: 8
    .kernarg_segment_size: 352
    .language:       OpenCL C
    .language_version:
      - 2
      - 0
    .max_flat_workgroup_size: 512
    .name:           _Z12layer_kernelILb1ELi512ELi64EEvPKDv8_DF16_PKfPS0_PiS6_S6_S2_S4_S5_PfPK15HIP_vector_typeIiLj2EEPKi
    .private_segment_fixed_size: 0
    .sgpr_count:     52
    .sgpr_spill_count: 0
    .symbol:         _Z12layer_kernelILb1ELi512ELi64EEvPKDv8_DF16_PKfPS0_PiS6_S6_S2_S4_S5_PfPK15HIP_vector_typeIiLj2EEPKi.kd
    .uniform_work_group_size: 1
    .uses_dynamic_stack: false
    .vgpr_count:     64
    .vgpr_spill_count: 0
    .wavefront_size: 64
  - .agpr_count:     0
    .args:
      - .actual_access:  read_only
        .address_space:  global
        .offset:         0
        .size:           8
        .value_kind:     global_buffer
      - .actual_access:  read_only
        .address_space:  global
        .offset:         8
        .size:           8
        .value_kind:     global_buffer
      - .actual_access:  read_only
        .address_space:  global
        .offset:         16
        .size:           8
        .value_kind:     global_buffer
      - .actual_access:  read_only
        .address_space:  global
        .offset:         24
        .size:           8
        .value_kind:     global_buffer
      - .actual_access:  read_only
        .address_space:  global
        .offset:         32
        .size:           8
        .value_kind:     global_buffer
      - .actual_access:  read_only
        .address_space:  global
        .offset:         40
        .size:           8
        .value_kind:     global_buffer
      - .actual_access:  read_only
        .address_space:  global
        .offset:         48
        .size:           8
        .value_kind:     global_buffer
      - .actual_access:  read_only
        .address_space:  global
        .offset:         56
        .size:           8
        .value_kind:     global_buffer
      - .address_space:  global
        .offset:         64
        .size:           8
        .value_kind:     global_buffer
      - .address_space:  global
        .offset:         72
        .size:           8
        .value_kind:     global_buffer
      - .actual_access:  read_only
        .address_space:  global
        .offset:         80
        .size:           8
        .value_kind:     global_buffer
      - .actual_access:  read_only
        .address_space:  global
        .offset:         88
        .size:           8
        .value_kind:     global_buffer
      - .offset:         96
        .size:           4
        .value_kind:     hidden_block_count_x
      - .offset:         100
        .size:           4
        .value_kind:     hidden_block_count_y
      - .offset:         104
        .size:           4
        .value_kind:     hidden_block_count_z
      - .offset:         108
        .size:           2
        .value_kind:     hidden_group_size_x
      - .offset:         110
        .size:           2
        .value_kind:     hidden_group_size_y
      - .offset:         112
        .size:           2
        .value_kind:     hidden_group_size_z
      - .offset:         114
        .size:           2
        .value_kind:     hidden_remainder_x
      - .offset:         116
        .size:           2
        .value_kind:     hidden_remainder_y
      - .offset:         118
        .size:           2
        .value_kind:     hidden_remainder_z
      - .offset:         136
        .size:           8
        .value_kind:     hidden_global_offset_x
      - .offset:         144
        .size:           8
        .value_kind:     hidden_global_offset_y
      - .offset:         152
        .size:           8
        .value_kind:     hidden_global_offset_z
      - .offset:         160
        .size:           2
        .value_kind:     hidden_grid_dims
    .group_segment_fixed_size: 12932
    .kernarg_segment_align: 8
    .kernarg_segment_size: 352
    .language:       OpenCL C
    .language_version:
      - 2
      - 0
    .max_flat_workgroup_size: 256
    .name:           _Z12layer_kernelILb0ELi256ELi32EEvPKDv8_DF16_PKfPS0_PiS6_S6_S2_S4_S5_PfPK15HIP_vector_typeIiLj2EEPKi
    .private_segment_fixed_size: 0
    .sgpr_count:     36
    .sgpr_spill_count: 0
    .symbol:         _Z12layer_kernelILb0ELi256ELi32EEvPKDv8_DF16_PKfPS0_PiS6_S6_S2_S4_S5_PfPK15HIP_vector_typeIiLj2EEPKi.kd
    .uniform_work_group_size: 1
    .uses_dynamic_stack: false
    .vgpr_count:     64
    .vgpr_spill_count: 0
    .wavefront_size: 64
